# non-temporal policy on the read-once row loads of the norm/residual phases (N0 x rows, N1 ymix/x rows, N2 yslot/xb rows)
# speedup vs baseline: 1.0084x; 1.0084x over previous
; DI const float* inp(kptr_t k, int i) { return (const float*)k[i]; }
; DI void phase_n0(Frame& F, int l) {
;     ...
;     for (int r0 = gw * 2; r0 < T; r0 += NGW * 2) {
;         f32x4 xa[2][4], hv[4];
; #pragma unroll
;         for (int rr = 0; rr < 2; ++rr) load_row_f32(inp(KA, I_X) + (size_t)(r0 + rr) * D, F.lane, xa[rr]);
;         ModP mp; { const int b = r0 / SEQ; load_modp(mp, inp(KA, I_GPREMIX) + l * D, mod + (size_t)b * NMOD * D + 1 * D, mod + (size_t)b * NMOD * D + 0 * D, F.lane); }
; #pragma unroll
;         for (int rr = 0; rr < 2; ++rr) { const int r = r0 + rr; const float rstd = rsqrtf(sumsq(xa[rr], F.lane) * (1.0f / D) + RMS_EPS);
;             mod_norm_store8(xa[rr], rstd, mp, F.ws + WS_HF8 + (size_t)r * D, F.lane, hv); }
.LBB0_180:
	s_ashr_i32 s4, s0, 31
	v_add_co_u32_e32 v44, vcc, 0xfffff000, v42
	s_lshr_b32 s4, s4, 21
	global_load_dwordx4 v[0:3], v[42:43], off offset:-4096 nt
	global_load_dwordx4 v[32:35], v[42:43], off offset:-3072 nt
	global_load_dwordx4 v[28:31], v[42:43], off offset:-2048 nt
	global_load_dwordx4 v[24:27], v[42:43], off offset:-1024 nt
	global_load_dwordx4 v[20:23], v[42:43], off nt
	v_addc_co_u32_e32 v45, vcc, -1, v43, vcc
	s_add_i32 s4, s0, s4
	global_load_dwordx4 v[4:7], v[38:39], off
	global_load_dwordx4 v[8:11], v[38:39], off offset:1024
	global_load_dwordx4 v[12:15], v[38:39], off offset:2048
	global_load_dwordx4 v[16:19], v[38:39], off offset:3072
	global_load_dwordx4 v[50:53], v[44:45], off offset:-3072 nt
	global_load_dwordx4 v[54:57], v[44:45], off offset:-2048 nt
	global_load_dwordx4 v[58:61], v[44:45], off offset:-1024 nt
	s_ashr_i32 s4, s4, 11
	s_mul_i32 s4, s4, 6
	s_ashr_i32 s5, s4, 31
	s_lshl_b64 s[4:5], s[4:5], 12
	s_add_u32 s4, s66, s4
	s_addc_u32 s5, s67, s5
	v_lshl_add_u64 v[44:45], v[36:37], 2, s[4:5]
	v_add_co_u32_e32 v96, vcc, s1, v44
	v_lshl_add_u64 v[94:95], v[44:45], 0, s[8:9]
	s_nop 0
	v_addc_co_u32_e32 v97, vcc, 0, v45, vcc
	global_load_dwordx4 v[62:65], v[44:45], off
	global_load_dwordx4 v[66:69], v[44:45], off offset:1024
	global_load_dwordx4 v[70:73], v[44:45], off offset:2048
	global_load_dwordx4 v[74:77], v[44:45], off offset:3072
	global_load_dwordx4 v[78:81], v[96:97], off
	global_load_dwordx4 v[82:85], v[94:95], off offset:1024
	global_load_dwordx4 v[86:89], v[94:95], off offset:2048
	global_load_dwordx4 v[90:93], v[94:95], off offset:3072
	v_mov_b32_e32 v113, 0
	v_mov_b32_e32 v115, 0
	v_mov_b32_e32 v119, 0
	v_mov_b32_e32 v49, 0
	v_mov_b32_e32 v120, 0
	v_mov_b32_e32 v121, 0
	v_mov_b32_e32 v122, 0
	v_mov_b32_e32 v123, 0
	v_mov_b32_e32 v124, 0
	v_mov_b32_e32 v116, 0
	v_mov_b32_e32 v117, 0
	v_mov_b32_e32 v118, 0
	s_add_i32 s0, s0, s36
	v_lshl_add_u64 v[42:43], v[42:43], 0, s[6:7]
	s_cmp_lt_i32 s0, 0x8000
	s_waitcnt vmcnt(19)
	v_mul_f32_e32 v125, v0, v0
	s_waitcnt vmcnt(18)
	v_pk_mul_f32 v[44:45], v[34:35], v[34:35]
	v_pk_mul_f32 v[94:95], v[32:33], v[32:33]
	s_waitcnt vmcnt(17)
	v_pk_mul_f32 v[96:97], v[30:31], v[30:31]
	v_pk_mul_f32 v[98:99], v[28:29], v[28:29]
	s_waitcnt vmcnt(16)
	v_mul_f32_e32 v100, v25, v25
	v_mul_f32_e32 v102, v27, v27
	v_pk_mov_b32 v[104:105], v[94:95], v[44:45] op_sel:[1,0]
	v_mov_b32_e32 v95, v45
	v_pk_mov_b32 v[44:45], v[98:99], v[96:97] op_sel:[1,0]
	v_mov_b32_e32 v99, v97
	s_waitcnt vmcnt(15)
	v_mul_f32_e32 v131, v22, v22
	v_mul_f32_e32 v132, v23, v23
	v_pk_fma_f32 v[96:97], v[24:25], v[24:25], v[100:101] op_sel_hi:[1,1,0]
	v_pk_fma_f32 v[100:101], v[26:27], v[26:27], v[102:103] op_sel_hi:[1,1,0]
	s_waitcnt vmcnt(10)
	v_pk_mul_f32 v[102:103], v[52:53], v[52:53]
	v_pk_mul_f32 v[106:107], v[50:51], v[50:51]
	s_waitcnt vmcnt(9)
	v_pk_mul_f32 v[108:109], v[56:57], v[56:57]
	v_pk_mul_f32 v[110:111], v[54:55], v[54:55]
	v_pk_add_f32 v[94:95], v[104:105], v[94:95]
	v_pk_add_f32 v[44:45], v[44:45], v[98:99]
	v_mul_f32_e32 v129, v20, v20
	v_mul_f32_e32 v130, v21, v21
	v_mov_b32_e32 v97, v131
	v_mov_b32_e32 v101, v132
	v_pk_mov_b32 v[98:99], v[106:107], v[102:103] op_sel:[1,0]
	v_mov_b32_e32 v107, v103
	v_pk_mov_b32 v[102:103], v[110:111], v[108:109] op_sel:[1,0]
	v_mov_b32_e32 v111, v109
	v_pk_add_f32 v[94:95], v[94:95], v[94:95] op_sel:[0,1] op_sel_hi:[1,0]
	v_pk_add_f32 v[44:45], v[44:45], v[44:45] op_sel:[0,1] op_sel_hi:[1,0]
	s_waitcnt vmcnt(8)
	v_mul_f32_e32 v112, v59, v59
	v_mul_f32_e32 v114, v61, v61
	v_pk_add_f32 v[96:97], v[96:97], v[100:101]
	v_pk_add_f32 v[98:99], v[98:99], v[106:107]
	v_pk_add_f32 v[100:101], v[102:103], v[110:111]
	v_mov_b32_e32 v95, v129
	v_mov_b32_e32 v45, v130
	v_mul_f32_e32 v126, v1, v1
	v_mul_f32_e32 v127, v2, v2
	v_mul_f32_e32 v128, v3, v3
	v_pk_fma_f32 v[104:105], v[58:59], v[58:59], v[112:113] op_sel_hi:[1,1,0]
	v_pk_fma_f32 v[108:109], v[60:61], v[60:61], v[114:115] op_sel_hi:[1,1,0]
	v_pk_add_f32 v[98:99], v[98:99], v[98:99] op_sel:[0,1] op_sel_hi:[1,0]
	v_pk_add_f32 v[100:101], v[100:101], v[100:101] op_sel:[0,1] op_sel_hi:[1,0]
	v_pk_add_f32 v[44:45], v[94:95], v[44:45]
	v_mov_b32_e32 v105, v127
	v_mov_b32_e32 v109, v128
	v_mov_b32_e32 v99, v125
	v_mov_b32_e32 v101, v126
	v_pk_add_f32 v[44:45], v[44:45], v[96:97]
	v_pk_add_f32 v[102:103], v[104:105], v[108:109]
	v_pk_add_f32 v[94:95], v[98:99], v[100:101]
	v_add_f32_e32 v96, v44, v45
	v_pk_add_f32 v[44:45], v[94:95], v[102:103]
	s_waitcnt vmcnt(3)
	v_pk_add_f32 v[78:79], v[78:79], 1.0 op_sel_hi:[1,0]
	v_add_f32_dpp v94, v96, v96 row_shr:1 row_mask:0xf bank_mask:0xf bound_ctrl:1
	v_add_f32_e32 v44, v44, v45
	s_waitcnt vmcnt(2)
	v_pk_add_f32 v[82:83], v[82:83], 1.0 op_sel_hi:[1,0]
	v_add_f32_dpp v45, v94, v94 row_shr:2 row_mask:0xf bank_mask:0xf bound_ctrl:1
	v_add_f32_dpp v94, v44, v44 row_shr:1 row_mask:0xf bank_mask:0xf bound_ctrl:1
	s_waitcnt vmcnt(1)
	v_pk_add_f32 v[86:87], v[86:87], 1.0 op_sel_hi:[1,0]
	v_add_f32_dpp v95, v45, v45 row_shr:4 row_mask:0xf bank_mask:0xf bound_ctrl:1
	v_pk_add_f32 v[44:45], v[80:81], 1.0 op_sel_hi:[1,0]
	v_pk_add_f32 v[80:81], v[84:85], 1.0 op_sel_hi:[1,0]
	v_pk_add_f32 v[84:85], v[88:89], 1.0 op_sel_hi:[1,0]
	s_waitcnt vmcnt(0)
; DI unsigned pk4_fp8(float a, float b, float c, float d) { int r = 0; r = __builtin_amdgcn_cvt_pk_fp8_f32(sat8(a), sat8(b), r, false); r = __builtin_amdgcn_cvt_pk_fp8_f32(sat8(c), sat8(d), r, true); return (unsigned)r; }
; #define DPP_ADD_(ctrl, rmask, bc) v += __int_as_float(__builtin_amdgcn_update_dpp(0, __float_as_int(v), ctrl, rmask, 0xf, bc))
; DI float wave_sum_dpp(float v) {
;     ...
;     DPP_ADD_(0x111, 0xf, true); DPP_ADD_(0x112, 0xf, true); DPP_ADD_(0x114, 0xf, true); DPP_ADD_(0x118, 0xf, true);
;     DPP_ADD_(0x142, 0xa, false); DPP_ADD_(0x143, 0xc, false);
;     ...
;     return __int_as_float(__builtin_amdgcn_readlane(__float_as_int(v), 63)); }
; #pragma unroll
;     for (int j = 0; j < 4; ++j) s += (v[j][0] * v[j][0] + v[j][1] * v[j][1]) + (v[j][2] * v[j][2] + v[j][3] * v[j][3]);
;     return wave_sum_dpp(s); }
; DI void mod_norm_store8(const f32x4 (&xv)[4], float rstd, const ModP& m, unsigned char* orow, int lane, f32x4 (&hv)[4]) {
; #pragma unroll
;     ...
;         hv[j] = xv[j] * rstd * gv * (1.0f + scv) + shv;
;         *(unsigned*)(orow + o) = pk4_fp8(hv[j][0] * H8_SCALE, hv[j][1] * H8_SCALE, hv[j][2] * H8_SCALE, hv[j][3] * H8_SCALE); }
; }
	v_pk_add_f32 v[88:89], v[92:93], 1.0 op_sel_hi:[1,0]
	v_add_f32_dpp v92, v94, v94 row_shr:2 row_mask:0xf bank_mask:0xf bound_ctrl:1
	v_add_f32_dpp v93, v95, v95 row_shr:8 row_mask:0xf bank_mask:0xf bound_ctrl:1
	v_pk_add_f32 v[90:91], v[90:91], 1.0 op_sel_hi:[1,0]
	v_add_f32_dpp v92, v92, v92 row_shr:4 row_mask:0xf bank_mask:0xf bound_ctrl:1
	v_mov_b32_dpp v119, v93 row_bcast:15 row_mask:0xa bank_mask:0xf
	v_add_f32_e32 v93, v93, v119
	v_add_f32_dpp v92, v92, v92 row_shr:8 row_mask:0xf bank_mask:0xf bound_ctrl:1
	s_nop 0
	v_mov_b32_dpp v120, v93 row_bcast:31 row_mask:0xc bank_mask:0xf
	v_mov_b32_dpp v49, v92 row_bcast:15 row_mask:0xa bank_mask:0xf
	v_add_f32_e32 v49, v92, v49
	v_add_f32_e32 v92, v93, v120
	s_nop 0
	v_mov_b32_dpp v113, v49 row_bcast:31 row_mask:0xc bank_mask:0xf
	v_readlane_b32 s4, v92, 63
	v_add_f32_e32 v49, v49, v113
	s_nop 0
	v_fma_f32 v92, s4, v47, v46
	v_readlane_b32 s4, v49, 63
	v_mul_f32_e32 v49, 0x4b800000, v92
	v_cmp_gt_f32_e32 vcc, s11, v92
	v_fma_f32 v93, s4, v47, v46
	v_cmp_gt_f32_e64 s[4:5], s11, v93
	v_cndmask_b32_e32 v49, v92, v49, vcc
	v_mul_f32_e32 v92, 0x4b800000, v93
	v_rsq_f32_e32 v49, v49
	v_cndmask_b32_e64 v92, v93, v92, s[4:5]
	v_rsq_f32_e32 v93, v92
	v_mul_f32_e32 v92, 0x45800000, v49
	v_cndmask_b32_e32 v92, v49, v92, vcc
	v_mul_f32_e32 v49, 0x45800000, v93
	v_pk_mul_f32 v[32:33], v[32:33], v[92:93] op_sel_hi:[1,0]
	v_pk_mul_f32 v[34:35], v[34:35], v[92:93] op_sel_hi:[1,0]
	v_pk_mul_f32 v[30:31], v[30:31], v[92:93] op_sel_hi:[1,0]
	v_pk_mul_f32 v[28:29], v[28:29], v[92:93] op_sel_hi:[1,0]
	v_pk_mul_f32 v[26:27], v[26:27], v[92:93] op_sel_hi:[1,0]
	v_pk_mul_f32 v[24:25], v[24:25], v[92:93] op_sel_hi:[1,0]
	v_pk_mul_f32 v[22:23], v[22:23], v[92:93] op_sel_hi:[1,0]
	v_pk_mul_f32 v[20:21], v[20:21], v[92:93] op_sel_hi:[1,0]
	v_cndmask_b32_e64 v92, v93, v49, s[4:5]
	v_pk_mul_f32 v[32:33], v[4:5], v[32:33]
	v_pk_mul_f32 v[28:29], v[8:9], v[28:29]
	v_pk_mul_f32 v[0:1], v[0:1], v[92:93] op_sel_hi:[1,0]
	v_pk_fma_f32 v[32:33], v[78:79], v[32:33], v[62:63]
	v_pk_mul_f32 v[24:25], v[12:13], v[24:25]
	v_pk_mul_f32 v[20:21], v[16:17], v[20:21]
	v_pk_fma_f32 v[28:29], v[82:83], v[28:29], v[66:67]
	v_pk_mul_f32 v[0:1], v[16:17], v[0:1]
	v_mul_f32_e32 v16, 0x41800000, v32
	v_mul_f32_e32 v17, 0x41800000, v33
	v_pk_mul_f32 v[50:51], v[50:51], v[92:93] op_sel_hi:[1,0]
	v_pk_mul_f32 v[54:55], v[54:55], v[92:93] op_sel_hi:[1,0]
	v_pk_mul_f32 v[58:59], v[58:59], v[92:93] op_sel_hi:[1,0]
	v_pk_fma_f32 v[24:25], v[86:87], v[24:25], v[70:71]
	v_mul_f32_e32 v28, 0x41800000, v28
	v_mul_f32_e32 v29, 0x41800000, v29
	v_med3_f32 v16, v16, s12, v48
	v_med3_f32 v17, v17, s12, v48
	v_pk_mul_f32 v[34:35], v[6:7], v[34:35]
	v_pk_fma_f32 v[20:21], v[90:91], v[20:21], v[74:75]
	v_pk_mul_f32 v[4:5], v[4:5], v[50:51]
	v_pk_mul_f32 v[8:9], v[8:9], v[54:55]
	v_pk_mul_f32 v[12:13], v[12:13], v[58:59]
	v_mul_f32_e32 v24, 0x41800000, v24
	v_mul_f32_e32 v25, 0x41800000, v25
	v_med3_f32 v28, v28, s12, v48
	v_med3_f32 v29, v29, s12, v48
	v_cvt_pk_fp8_f32 v121, v16, v17
	v_pk_mul_f32 v[30:31], v[10:11], v[30:31]
	v_pk_mul_f32 v[2:3], v[2:3], v[92:93] op_sel_hi:[1,0]
	v_pk_fma_f32 v[34:35], v[44:45], v[34:35], v[64:65]
	v_mul_f32_e32 v20, 0x41800000, v20
	v_mul_f32_e32 v21, 0x41800000, v21
	v_pk_fma_f32 v[4:5], v[78:79], v[4:5], v[62:63]
	v_pk_fma_f32 v[8:9], v[82:83], v[8:9], v[66:67]
	v_pk_fma_f32 v[12:13], v[86:87], v[12:13], v[70:71]
	v_pk_fma_f32 v[0:1], v[90:91], v[0:1], v[74:75]
	v_med3_f32 v24, v24, s12, v48
	v_med3_f32 v25, v25, s12, v48
	v_cvt_pk_fp8_f32 v122, v28, v29
	v_pk_mul_f32 v[26:27], v[14:15], v[26:27]
	v_pk_mul_f32 v[22:23], v[18:19], v[22:23]
	v_pk_fma_f32 v[30:31], v[80:81], v[30:31], v[68:69]
	v_pk_mul_f32 v[2:3], v[18:19], v[2:3]
	v_mul_f32_e32 v18, 0x41800000, v34
	v_mul_f32_e32 v19, 0x41800000, v35
	v_med3_f32 v20, v20, s12, v48
	v_med3_f32 v21, v21, s12, v48
	v_mul_f32_e32 v4, 0x41800000, v4
	v_mul_f32_e32 v5, 0x41800000, v5
	v_mul_f32_e32 v8, 0x41800000, v8
	v_mul_f32_e32 v9, 0x41800000, v9
	v_mul_f32_e32 v12, 0x41800000, v12
	v_mul_f32_e32 v13, 0x41800000, v13
	v_mul_f32_e32 v0, 0x41800000, v0
	v_mul_f32_e32 v1, 0x41800000, v1
	v_cvt_pk_fp8_f32 v123, v24, v25
	v_pk_mul_f32 v[52:53], v[52:53], v[92:93] op_sel_hi:[1,0]
	v_pk_mul_f32 v[56:57], v[56:57], v[92:93] op_sel_hi:[1,0]
	v_pk_mul_f32 v[60:61], v[60:61], v[92:93] op_sel_hi:[1,0]
	v_pk_fma_f32 v[26:27], v[84:85], v[26:27], v[72:73]
	v_mul_f32_e32 v30, 0x41800000, v30
	v_mul_f32_e32 v31, 0x41800000, v31
	v_med3_f32 v18, v18, s12, v48
	v_med3_f32 v19, v19, s12, v48
	v_cvt_pk_fp8_f32 v124, v20, v21
	v_med3_f32 v4, v4, s12, v48
	v_med3_f32 v5, v5, s12, v48
	v_med3_f32 v8, v8, s12, v48
	v_med3_f32 v9, v9, s12, v48
	v_med3_f32 v12, v12, s12, v48
	v_med3_f32 v13, v13, s12, v48
	v_med3_f32 v0, v0, s12, v48
	v_med3_f32 v1, v1, s12, v48
	v_pk_fma_f32 v[22:23], v[88:89], v[22:23], v[76:77]
	v_pk_mul_f32 v[6:7], v[6:7], v[52:53]
	v_pk_mul_f32 v[10:11], v[10:11], v[56:57]
	v_pk_mul_f32 v[14:15], v[14:15], v[60:61]
	v_mul_f32_e32 v26, 0x41800000, v26
	v_mul_f32_e32 v27, 0x41800000, v27
	v_med3_f32 v30, v30, s12, v48
	v_med3_f32 v31, v31, s12, v48
	v_cvt_pk_fp8_f32 v115, v4, v5
	v_cvt_pk_fp8_f32 v116, v8, v9
	v_cvt_pk_fp8_f32 v117, v12, v13
	v_cvt_pk_fp8_f32 v118, v0, v1
	v_cvt_pk_fp8_f32 v121, v18, v19 op_sel:[0,0,1]
	v_mul_f32_e32 v22, 0x41800000, v22
	v_mul_f32_e32 v23, 0x41800000, v23
	v_pk_fma_f32 v[6:7], v[44:45], v[6:7], v[64:65]
	v_pk_fma_f32 v[10:11], v[80:81], v[10:11], v[68:69]
	v_pk_fma_f32 v[14:15], v[84:85], v[14:15], v[72:73]
	v_pk_fma_f32 v[2:3], v[88:89], v[2:3], v[76:77]
	v_med3_f32 v26, v26, s12, v48
	v_med3_f32 v27, v27, s12, v48
	v_cvt_pk_fp8_f32 v122, v30, v31 op_sel:[0,0,1]
	v_med3_f32 v22, v22, s12, v48
	v_med3_f32 v23, v23, s12, v48
	v_mul_f32_e32 v6, 0x41800000, v6
	v_mul_f32_e32 v7, 0x41800000, v7
	v_mul_f32_e32 v10, 0x41800000, v10
	v_mul_f32_e32 v11, 0x41800000, v11
	v_mul_f32_e32 v14, 0x41800000, v14
	v_mul_f32_e32 v15, 0x41800000, v15
	v_mul_f32_e32 v2, 0x41800000, v2
	v_mul_f32_e32 v3, 0x41800000, v3
	v_cvt_pk_fp8_f32 v123, v26, v27 op_sel:[0,0,1]
	v_med3_f32 v6, v6, s12, v48
	v_med3_f32 v7, v7, s12, v48
	v_med3_f32 v10, v10, s12, v48
	v_med3_f32 v11, v11, s12, v48
	v_med3_f32 v14, v14, s12, v48
	v_med3_f32 v15, v15, s12, v48
	v_med3_f32 v2, v2, s12, v48
	v_med3_f32 v3, v3, s12, v48
	v_cvt_pk_fp8_f32 v124, v22, v23 op_sel:[0,0,1]
	v_cvt_pk_fp8_f32 v115, v6, v7 op_sel:[0,0,1]
	v_cvt_pk_fp8_f32 v116, v10, v11 op_sel:[0,0,1]
	v_cvt_pk_fp8_f32 v117, v14, v15 op_sel:[0,0,1]
	v_cvt_pk_fp8_f32 v118, v2, v3 op_sel:[0,0,1]
	global_store_dword v[40:41], v121, off offset:-768
	global_store_dword v[40:41], v122, off offset:-512
	global_store_dword v[40:41], v123, off offset:-256
	global_store_dword v[40:41], v124, off
	global_store_dword v[40:41], v115, off offset:-1792
	global_store_dword v[40:41], v116, off offset:-1536
	global_store_dword v[40:41], v117, off offset:-1280
	global_store_dword v[40:41], v118, off offset:-1024
	v_lshl_add_u64 v[40:41], v[40:41], 0, s[2:3]
	s_cbranch_scc1 .LBB0_180

; DI void phase_n1(Frame& F, int l) {
;     ...
;     for (int blk = F.bid; blk < T / 16; blk += F.G) {
;         if (F.tid < 32) hist[F.tid] = 0;
;         f32x4 hv[2][4], yv2[2][4], xv2[2][4];
; #pragma unroll
;         for (int rr = 0; rr < 2; ++rr) { const int r = blk * 16 + F.wave * 2 + rr;
;             load_row_bf16(ymix + (size_t)r * D, F.lane, yv2[rr]); if (l == 0) load_row_f32(xin + (size_t)r * D, F.lane, xv2[rr]); else load_row_bf16(xb + (size_t)r * D, F.lane, xv2[rr]); }
.LBB0_1030:
	s_and_saveexec_b64 s[2:3], s[4:5]
	ds_write_b32 v147, v1
	s_or_b64 exec, exec, s[2:3]
	s_ashr_i32 s23, s22, 31
	s_lshl_b64 s[28:29], s[22:23], 11
	v_lshl_add_u64 v[2:3], v[98:99], 0, s[28:29]
	global_load_dwordx2 v[24:25], v[2:3], off nt
	global_load_dwordx2 v[22:23], v[2:3], off offset:512 nt
	global_load_dwordx2 v[20:21], v[2:3], off offset:1024 nt
	global_load_dwordx2 v[18:19], v[2:3], off offset:1536 nt
	v_readlane_b32 s0, v253, 23
	v_readlane_b32 s1, v253, 24
	s_lshl_b64 s[26:27], s[22:23], 10
	s_mov_b64 s[2:3], -1
	s_and_b64 vcc, exec, s[0:1]
	s_cbranch_vccz .LBB0_1034
	v_lshl_add_u64 v[2:3], s[26:27], 1, v[100:101]
	global_load_dwordx2 v[4:5], v[2:3], off nt
	global_load_dwordx2 v[6:7], v[2:3], off offset:512 nt
	global_load_dwordx2 v[8:9], v[2:3], off offset:1024 nt
	s_nop 0
	global_load_dwordx2 v[2:3], v[2:3], off offset:1536 nt
	s_mov_b64 s[2:3], 0
	s_waitcnt vmcnt(0)
	v_lshlrev_b32_e32 v62, 16, v4
	v_and_b32_e32 v63, 0xffff0000, v4
	v_lshlrev_b32_e32 v64, 16, v5
	v_and_b32_e32 v65, 0xffff0000, v5
	v_lshlrev_b32_e32 v58, 16, v6
	v_and_b32_e32 v59, 0xffff0000, v6
	v_lshlrev_b32_e32 v60, 16, v7
	v_and_b32_e32 v61, 0xffff0000, v7
	v_lshlrev_b32_e32 v50, 16, v8
	v_and_b32_e32 v51, 0xffff0000, v8
	v_lshlrev_b32_e32 v52, 16, v9
	v_and_b32_e32 v53, 0xffff0000, v9
	v_lshlrev_b32_e32 v38, 16, v2
	v_and_b32_e32 v39, 0xffff0000, v2
	v_lshlrev_b32_e32 v40, 16, v3
	v_and_b32_e32 v41, 0xffff0000, v3
.LBB0_1034:
	s_andn2_b64 vcc, exec, s[2:3]
	s_cbranch_vccnz .LBB0_1036
	v_lshl_add_u64 v[2:3], s[26:27], 2, v[102:103]
	global_load_dwordx4 v[62:65], v[2:3], off nt
	global_load_dwordx4 v[58:61], v[2:3], off offset:1024 nt
	global_load_dwordx4 v[50:53], v[2:3], off offset:2048 nt
	global_load_dwordx4 v[38:41], v[2:3], off offset:3072 nt
.LBB0_1036:
	s_add_i32 s0, s22, 1
	s_ashr_i32 s1, s0, 31
	s_lshl_b64 s[14:15], s[0:1], 11
	v_lshl_add_u64 v[2:3], v[98:99], 0, s[14:15]
	global_load_dwordx2 v[32:33], v[2:3], off nt
	global_load_dwordx2 v[30:31], v[2:3], off offset:512 nt
	global_load_dwordx2 v[28:29], v[2:3], off offset:1024 nt
	global_load_dwordx2 v[26:27], v[2:3], off offset:1536 nt
	s_lshl_b64 s[2:3], s[0:1], 10
	v_readlane_b32 s0, v253, 23
	v_readlane_b32 s1, v253, 24
	s_andn2_b64 vcc, exec, s[0:1]
	s_mov_b64 s[16:17], -1
	s_cbranch_vccnz .LBB0_1038
	v_lshl_add_u64 v[2:3], s[2:3], 1, v[100:101]
	global_load_dwordx2 v[4:5], v[2:3], off nt
	global_load_dwordx2 v[6:7], v[2:3], off offset:512 nt
	global_load_dwordx2 v[8:9], v[2:3], off offset:1024 nt
	global_load_dwordx2 v[34:35], v[2:3], off offset:1536 nt
	s_mov_b64 s[16:17], 0
	s_waitcnt vmcnt(0)
	v_lshlrev_b32_e32 v14, 16, v4
	v_and_b32_e32 v15, 0xffff0000, v4
	v_lshlrev_b32_e32 v16, 16, v5
	v_and_b32_e32 v17, 0xffff0000, v5
	v_lshlrev_b32_e32 v10, 16, v6
	v_and_b32_e32 v11, 0xffff0000, v6
	v_lshlrev_b32_e32 v12, 16, v7
	v_and_b32_e32 v13, 0xffff0000, v7
	v_lshlrev_b32_e32 v6, 16, v8
	v_and_b32_e32 v7, 0xffff0000, v8
	v_lshlrev_b32_e32 v8, 16, v9
	v_and_b32_e32 v9, 0xffff0000, v9
	v_lshlrev_b32_e32 v2, 16, v34
	v_and_b32_e32 v3, 0xffff0000, v34
	v_lshlrev_b32_e32 v4, 16, v35
	v_and_b32_e32 v5, 0xffff0000, v35
.LBB0_1038:
	s_andn2_b64 vcc, exec, s[16:17]
	s_cbranch_vccnz .LBB0_1040
	v_lshl_add_u64 v[2:3], s[2:3], 2, v[102:103]
	global_load_dwordx4 v[14:17], v[2:3], off nt
	global_load_dwordx4 v[10:13], v[2:3], off offset:1024 nt
	global_load_dwordx4 v[6:9], v[2:3], off offset:2048 nt
	s_nop 0
	global_load_dwordx4 v[2:5], v[2:3], off offset:3072 nt

; DI const float* inp(kptr_t k, int i) { return (const float*)k[i]; }
; DI void phase_n2(Frame& F, int l) {
;     ...
;     for (int r0 = gw * 2; r0 < T; r0 += NGW * 2) {
;         f32x4 ya[2][4][4], xa[2][4];
; #pragma unroll
;         for (int rr = 0; rr < 2; ++rr) { const int r = r0 + rr;
; #pragma unroll
;             for (int k = 0; k < 4; ++k) load_row_fp8(ys + ((size_t)r * 4 + k) * D, F.lane, ya[rr][k]);
;             load_row_bf16(xb + (size_t)r * D, F.lane, xa[rr]); }
;         const float* mb = mod + (size_t)(r0 / SEQ) * NMOD * D;
;         f32x4 gpf[4], gtf[4]; ModP mp;
; #pragma unroll
;         for (int j = 0; j < 4; ++j) { const int o = 4 * F.lane + 256 * j; gpf[j] = *(const f32x4*)(inp(KA, I_GPOSTFFN) + l * D + o); gtf[j] = *(const f32x4*)(mb + 5 * D + o); }
;         if (l + 1 < DEPTH) { const float* mb2 = mb + (size_t)NB * NMOD * D; load_modp(mp, inp(KA, I_GPREMIX) + (l + 1) * D, mb2 + 1 * D, mb2 + 0 * D, F.lane); }
.LBB0_1400:
	v_readlane_b32 s0, v253, 8
	v_readlane_b32 s2, v253, 10
	v_readlane_b32 s3, v253, 11
	s_mov_b32 s0, 0x53a00000
	v_readlane_b32 s1, v253, 9
	v_lshl_add_u64 v[50:51], s[2:3], 0, v[110:111]
	v_add_co_u32_e32 v52, vcc, s0, v50
	s_mov_b32 s0, 0x53a01000
	s_nop 0
	v_addc_co_u32_e32 v53, vcc, 0, v51, vcc
	v_add_co_u32_e32 v50, vcc, s0, v50
	v_lshl_add_u64 v[112:113], s[2:3], 0, v[106:107]
	s_nop 0
	v_addc_co_u32_e32 v51, vcc, 0, v51, vcc
	s_mov_b32 s0, 0x63a00000
	v_add_co_u32_e32 v54, vcc, s0, v112
	global_load_dword v123, v[52:53], off offset:256 nt
	global_load_dword v97, v[52:53], off offset:512 nt
	global_load_dword v93, v[52:53], off offset:768 nt
	global_load_dword v92, v[52:53], off offset:1024 nt
	global_load_dword v89, v[52:53], off offset:1280 nt
	global_load_dword v88, v[52:53], off offset:1536 nt
	global_load_dword v85, v[52:53], off offset:1792 nt
	global_load_dword v84, v[52:53], off offset:2048 nt
	v_addc_co_u32_e32 v55, vcc, 0, v113, vcc
	global_load_dword v128, v[52:53], off offset:2304 nt
	global_load_dword v127, v[52:53], off offset:2560 nt
	global_load_dword v126, v[52:53], off offset:2816 nt
	global_load_dword v125, v[52:53], off offset:3072 nt
	global_load_dword v124, v[52:53], off offset:3328 nt
	global_load_dword v122, v[52:53], off offset:3584 nt
	global_load_dword v96, v[52:53], off offset:3840 nt
	global_load_dwordx2 v[82:83], v[54:55], off nt
	global_load_dword v129, v[50:51], off offset:-4096 nt
	global_load_dword v152, v[50:51], off nt
	global_load_dword v151, v[50:51], off offset:256 nt
	global_load_dword v150, v[50:51], off offset:512 nt
	global_load_dword v149, v[50:51], off offset:768 nt
	global_load_dword v148, v[50:51], off offset:1024 nt
	global_load_dword v147, v[50:51], off offset:1280 nt
	global_load_dword v146, v[50:51], off offset:1536 nt
	global_load_dword v145, v[50:51], off offset:1792 nt
	global_load_dword v144, v[50:51], off offset:2048 nt
	global_load_dword v143, v[50:51], off offset:2304 nt
	global_load_dword v142, v[50:51], off offset:2560 nt
	global_load_dword v141, v[50:51], off offset:2816 nt
	global_load_dword v140, v[50:51], off offset:3072 nt
	global_load_dword v139, v[50:51], off offset:3328 nt
	global_load_dword v138, v[50:51], off offset:3584 nt
	global_load_dword v0, v[50:51], off offset:3840 nt
	global_load_dwordx2 v[86:87], v[54:55], off offset:512 nt
	global_load_dwordx2 v[90:91], v[54:55], off offset:1024 nt
	global_load_dwordx2 v[94:95], v[54:55], off offset:1536 nt
	global_load_dwordx2 v[120:121], v[54:55], off offset:2048 nt
	global_load_dwordx2 v[118:119], v[54:55], off offset:2560 nt
	global_load_dwordx2 v[116:117], v[54:55], off offset:3072 nt
	global_load_dwordx2 v[114:115], v[54:55], off offset:3584 nt
	s_ashr_i32 s0, s10, 31
	s_lshr_b32 s0, s0, 21
	s_add_i32 s0, s10, s0
	s_ashr_i32 s0, s0, 11
	s_mul_i32 s0, s0, 6
	s_ashr_i32 s1, s0, 31
	s_lshl_b64 s[0:1], s[0:1], 12
	s_add_u32 s2, s12, s0
	s_addc_u32 s3, s13, s1
	v_lshl_add_u64 v[50:51], v[98:99], 2, s[2:3]
	s_mov_b64 s[0:1], 0x5000
	v_lshl_add_u64 v[52:53], v[50:51], 0, s[0:1]
	v_add_co_u32_e32 v50, vcc, 0x5000, v50
	v_readlane_b32 s0, v253, 17
	s_nop 0
	v_addc_co_u32_e32 v51, vcc, 0, v51, vcc
	global_load_dwordx4 v[74:77], v[102:103], off
	global_load_dwordx4 v[70:73], v[102:103], off offset:1024
	global_load_dwordx4 v[66:69], v[52:53], off offset:1024
	global_load_dwordx4 v[58:61], v[52:53], off offset:2048
	global_load_dwordx4 v[62:65], v[102:103], off offset:2048
	global_load_dwordx4 v[54:57], v[102:103], off offset:3072
	global_load_dwordx4 v[78:81], v[50:51], off
	s_nop 0
	global_load_dwordx4 v[50:53], v[52:53], off offset:3072
	v_readlane_b32 s1, v253, 18
	s_andn2_b64 vcc, exec, s[0:1]
	s_nop 0
	v_cndmask_b32_e64 v130, 0, 1, s[0:1]
	v_cmp_ne_u32_e64 s[4:5], 1, v130
	s_cbranch_vccnz .LBB0_1402
	s_load_dwordx2 s[0:1], s[8:9], 0x28
	v_lshl_add_u64 v[2:3], s[2:3], 0, v[100:101]
	s_waitcnt lgkmcnt(0)
	v_lshl_add_u64 v[4:5], s[0:1], 0, v[100:101]
	v_add_co_u32_e32 v18, vcc, 0x1000, v4
	s_mov_b64 s[0:1], 0x1000
	s_nop 0
	v_addc_co_u32_e32 v19, vcc, 0, v5, vcc
	v_add_co_u32_e32 v30, vcc, 0x61000, v2
	v_lshl_add_u64 v[22:23], v[4:5], 0, s[0:1]
	s_nop 0
	v_addc_co_u32_e32 v31, vcc, 0, v3, vcc
	s_mov_b64 s[0:1], 0x61000
	v_add_co_u32_e32 v32, vcc, 0x60000, v2
	v_lshl_add_u64 v[24:25], v[2:3], 0, s[0:1]
	s_mov_b64 s[0:1], 0x60000
	v_addc_co_u32_e32 v33, vcc, 0, v3, vcc
	v_lshl_add_u64 v[130:131], v[2:3], 0, s[0:1]
	global_load_dwordx4 v[2:5], v[22:23], off offset:1024
	global_load_dwordx4 v[14:17], v[22:23], off offset:2048
	global_load_dwordx4 v[26:29], v[24:25], off offset:1024
	global_load_dwordx4 v[34:37], v[24:25], off offset:2048
	global_load_dwordx4 v[10:13], v[130:131], off offset:1024
	global_load_dwordx4 v[6:9], v[130:131], off offset:2048
	s_nop 0
	global_load_dwordx4 v[18:21], v[18:19], off
	s_nop 0
	global_load_dwordx4 v[38:41], v[22:23], off offset:3072
	global_load_dwordx4 v[42:45], v[30:31], off
	global_load_dwordx4 v[46:49], v[24:25], off offset:3072
	s_nop 0
	global_load_dwordx4 v[30:33], v[32:33], off
	s_nop 0
	global_load_dwordx4 v[22:25], v[130:131], off offset:3072
